# v49 + out-of-line near-tie blocks + aligned phase entries + LDS-atomic histogram
# speedup vs baseline: 1.0217x; 1.0123x over previous
.Lg_nocopy:
	v_mov_b32_e32 v97, 1
	v_and_b32_e32 v138, 15, v0
	v_or_b32_e32 v134, s24, v138
	v_lshlrev_b32_e32 v135, 3, v1
	v_lshlrev_b32_e32 v139, 2, v1
	v_bfe_u32 v140, v0, 4, 2
	v_cmp_eq_u32_e64 s[2:3], 0, v1
	.p2align 6
